# V sweep: packed weight word read from LDS three batches ahead in the slot's issue section; per-batch LDS wait removed
# baseline (speedup 1.0000x reference)
; #define LAS __attribute__((address_space(3)))
; #define LDS_WAIT() asm volatile("s_waitcnt lgkmcnt(0)" ::: "memory")
;     ...
;     LDS_WAIT(); asm volatile("" ::: "memory");
;     float wsj[PE_NT];
; #pragma unroll
;     for (int j = 0; j < PE_NT; ++j) {
;         LAS unsigned* lt = lw + j * PE_TOK_W + 128;
;         const float a0 = __builtin_bit_cast(float, lt[2 * lane]), a1 = __builtin_bit_cast(float, lt[2 * lane + 1]);
;         const float wm = fmaxf(wave_max(fmaxf(fabsf(a0), fabsf(a1))), 1e-30f), wq = 127.0f * __builtin_amdgcn_rcpf(wm);
;         wsj[j] = wm * (1.0f / 127.0f);
;         const unsigned pr = (__builtin_bit_cast(unsigned, __builtin_fmaf(a0, wq, 12582912.0f)) & 0xffu) | ((__builtin_bit_cast(unsigned, __builtin_fmaf(a1, wq, 12582912.0f)) & 0xffu) << 8);
;         const unsigned nbp = (unsigned)__builtin_amdgcn_update_dpp(0, (int)pr, 0xB1, 0xF, 0xF, true);
;         asm volatile("" ::: "memory");
;         if ((lane & 1) == 0) lt[2 * lane] = pr | (nbp << 16);
;     }
.LBB0_2861:
	s_waitcnt vmcnt(0)
	s_waitcnt vmcnt(0)
	s_waitcnt vmcnt(0)
	s_waitcnt lgkmcnt(0)
	v_add_u32_e32 v1, s90, v118
	ds_read_b64 v[126:127], v1
	ds_read_b64 v[128:129], v1 offset:1024
	ds_read_b64 v[2:3], v1 offset:512
	s_mov_b32 s0, 0xc0c0500
	v_and_b32_e32 v5, 1, v50
	v_cmp_eq_u32_e32 vcc, 0, v5
	s_waitcnt lgkmcnt(0)
	v_cvt_f32_i32_e32 v126, v126
	v_cvt_f32_i32_e32 v127, v127
	v_mul_f32_e32 v126, v128, v126
	v_mul_f32_e32 v127, v129, v127
	v_mul_f32_e32 v94, v126, v126
	v_mul_f32_e32 v95, v127, v127
	v_fmamk_f32 v94, v94, 0xbdd2d3e8, v113
	v_fmamk_f32 v95, v95, 0xbdd2d3e8, v113
	v_mul_f32_e32 v94, v126, v94
	v_mul_f32_e32 v95, v127, v95
	v_exp_f32_e32 v94, v94
	v_exp_f32_e32 v95, v95
	s_nop 0
	v_add_f32_e32 v94, 1.0, v94
	v_add_f32_e32 v95, 1.0, v95
	v_rcp_f32_e32 v94, v94
	v_rcp_f32_e32 v95, v95
	s_nop 0
	v_mul_f32_e32 v126, v126, v94
	v_mul_f32_e32 v127, v127, v95
	v_mul_f32_e32 v2, v2, v126
	v_mul_f32_e32 v3, v3, v127
	v_max_f32_e64 v0, |v3|, |v3|
	v_max_f32_e64 v4, |v2|, |v2|
	v_max_f32_e32 v0, v4, v0
	s_nop 1
	v_mov_b32_dpp v4, v0 quad_perm:[1,0,3,2] row_mask:0xf bank_mask:0xf bound_ctrl:1
	v_max_f32_e32 v4, v4, v4
	v_max_f32_e32 v0, v0, v4
	s_nop 1
	v_mov_b32_dpp v4, v0 quad_perm:[2,3,0,1] row_mask:0xf bank_mask:0xf bound_ctrl:1
	v_max_f32_e32 v4, v4, v4
	v_max_f32_e32 v0, v0, v4
	s_nop 1
	v_mov_b32_dpp v4, v0 row_half_mirror row_mask:0xf bank_mask:0xf bound_ctrl:1
	v_max_f32_e32 v4, v4, v4
	v_max_f32_e32 v0, v0, v4
	s_nop 1
	v_mov_b32_dpp v4, v0 row_mirror row_mask:0xf bank_mask:0xf bound_ctrl:1
	v_max_f32_e32 v4, v4, v4
	v_max_f32_e32 v0, v0, v4
	v_mov_b32_e32 v4, v0
	s_nop 1
	v_permlane16_swap_b32_e32 v0, v4
	v_max_f32 v0, v0, v4
	s_nop 1
	s_nop 0
	v_mov_b32_e32 v4, v0
	s_nop 1
	v_permlane32_swap_b32_e32 v0, v4
	v_max_f32 v0, v0, v4
	s_nop 0
	v_max_f32_e32 v0, v0, v0
	v_max_f32_e32 v0, 0xda24260, v0
	v_rcp_f32_e32 v4, v0
	s_nop 0
	v_mul_f32_e32 v4, 0x42fe0000, v4
	v_fmaak_f32 v3, v3, v4, 0x4b400000
	v_fmaak_f32 v2, v2, v4, 0x4b400000
	v_lshlrev_b32_e32 v3, 8, v3
	v_perm_b32 v2, v3, v2, s0
	s_nop 1
	v_mov_b32_dpp v3, v2 quad_perm:[1,0,3,2] row_mask:0xf bank_mask:0xf bound_ctrl:1
	s_and_saveexec_b64 s[0:1], vcc
	v_lshl_or_b32 v2, v3, 16, v2
	ds_write_b32 v1, v2 offset:512
	s_or_b64 exec, exec, s[0:1]
	ds_read_b64 v[126:127], v1 offset:1680
	ds_read_b64 v[128:129], v1 offset:2704
	ds_read_b64 v[4:5], v1 offset:2192
	s_mov_b32 s0, 0xc0c0500
	s_waitcnt lgkmcnt(0)
	v_cvt_f32_i32_e32 v126, v126
	v_cvt_f32_i32_e32 v127, v127
	v_mul_f32_e32 v126, v128, v126
	v_mul_f32_e32 v127, v129, v127
	v_mul_f32_e32 v94, v126, v126
	v_mul_f32_e32 v95, v127, v127
	v_fmamk_f32 v94, v94, 0xbdd2d3e8, v113
	v_fmamk_f32 v95, v95, 0xbdd2d3e8, v113
	v_mul_f32_e32 v94, v126, v94
	v_mul_f32_e32 v95, v127, v95
	v_exp_f32_e32 v94, v94
	v_exp_f32_e32 v95, v95
	s_nop 0
	v_add_f32_e32 v94, 1.0, v94
	v_add_f32_e32 v95, 1.0, v95
	v_rcp_f32_e32 v94, v94
	v_rcp_f32_e32 v95, v95
	s_nop 0
	v_mul_f32_e32 v126, v126, v94
	v_mul_f32_e32 v127, v127, v95
	v_mul_f32_e32 v4, v4, v126
	v_mul_f32_e32 v5, v5, v127
	v_max_f32_e64 v2, |v5|, |v5|
	v_max_f32_e64 v3, |v4|, |v4|
	v_max_f32_e32 v2, v3, v2
	s_nop 1
	v_mov_b32_dpp v3, v2 quad_perm:[1,0,3,2] row_mask:0xf bank_mask:0xf bound_ctrl:1
	v_max_f32_e32 v3, v3, v3
	v_max_f32_e32 v2, v2, v3
	s_nop 1
	v_mov_b32_dpp v3, v2 quad_perm:[2,3,0,1] row_mask:0xf bank_mask:0xf bound_ctrl:1
	v_max_f32_e32 v3, v3, v3
	v_max_f32_e32 v2, v2, v3
	s_nop 1
	v_mov_b32_dpp v3, v2 row_half_mirror row_mask:0xf bank_mask:0xf bound_ctrl:1
	v_max_f32_e32 v3, v3, v3
	v_max_f32_e32 v2, v2, v3
	s_nop 1
	v_mov_b32_dpp v3, v2 row_mirror row_mask:0xf bank_mask:0xf bound_ctrl:1
	v_max_f32_e32 v3, v3, v3
	v_max_f32_e32 v2, v2, v3
	v_mov_b32_e32 v3, v2
	s_nop 1
	v_permlane16_swap_b32_e32 v2, v3
	v_max_f32 v2, v2, v3
	s_nop 1
	s_nop 0
	v_mov_b32_e32 v3, v2
	s_nop 1
	v_permlane32_swap_b32_e32 v2, v3
	v_max_f32 v2, v2, v3
	s_nop 0
	v_max_f32_e32 v2, v2, v2
	v_max_f32_e32 v2, 0xda24260, v2
	v_rcp_f32_e32 v3, v2
	s_nop 0
	v_mul_f32_e32 v3, 0x42fe0000, v3
	v_fmaak_f32 v4, v4, v3, 0x4b400000
	v_fmaak_f32 v3, v5, v3, 0x4b400000
	v_lshlrev_b32_e32 v3, 8, v3
	v_perm_b32 v3, v3, v4, s0
	s_nop 1
	v_mov_b32_dpp v4, v3 quad_perm:[1,0,3,2] row_mask:0xf bank_mask:0xf bound_ctrl:1
	s_and_saveexec_b64 s[0:1], vcc
	v_lshl_or_b32 v3, v4, 16, v3
	ds_write_b32 v1, v3 offset:2192
	s_or_b64 exec, exec, s[0:1]
	ds_read_b64 v[126:127], v1 offset:3360
	ds_read_b64 v[128:129], v1 offset:4384
	ds_read_b64 v[4:5], v1 offset:3872
	s_mov_b32 s0, 0xc0c0500
	s_waitcnt lgkmcnt(0)
	v_cvt_f32_i32_e32 v126, v126
	v_cvt_f32_i32_e32 v127, v127
	v_mul_f32_e32 v126, v128, v126
	v_mul_f32_e32 v127, v129, v127
	v_mul_f32_e32 v94, v126, v126
	v_mul_f32_e32 v95, v127, v127
	v_fmamk_f32 v94, v94, 0xbdd2d3e8, v113
	v_fmamk_f32 v95, v95, 0xbdd2d3e8, v113
	v_mul_f32_e32 v94, v126, v94
	v_mul_f32_e32 v95, v127, v95
	v_exp_f32_e32 v94, v94
	v_exp_f32_e32 v95, v95
	s_nop 0
	v_add_f32_e32 v94, 1.0, v94
	v_add_f32_e32 v95, 1.0, v95
	v_rcp_f32_e32 v94, v94
	v_rcp_f32_e32 v95, v95
	s_nop 0
	v_mul_f32_e32 v126, v126, v94
	v_mul_f32_e32 v127, v127, v95
	v_mul_f32_e32 v4, v4, v126
	v_mul_f32_e32 v5, v5, v127
	v_max_f32_e64 v3, |v5|, |v5|
	v_max_f32_e64 v6, |v4|, |v4|
	v_max_f32_e32 v3, v6, v3
	s_nop 1
	v_mov_b32_dpp v6, v3 quad_perm:[1,0,3,2] row_mask:0xf bank_mask:0xf bound_ctrl:1
	v_max_f32_e32 v6, v6, v6
	v_max_f32_e32 v3, v3, v6
	s_nop 1
	v_mov_b32_dpp v6, v3 quad_perm:[2,3,0,1] row_mask:0xf bank_mask:0xf bound_ctrl:1
	v_max_f32_e32 v6, v6, v6
	v_max_f32_e32 v3, v3, v6
	s_nop 1
	v_mov_b32_dpp v6, v3 row_half_mirror row_mask:0xf bank_mask:0xf bound_ctrl:1
	v_max_f32_e32 v6, v6, v6
	v_max_f32_e32 v3, v3, v6
	s_nop 1
	v_mov_b32_dpp v6, v3 row_mirror row_mask:0xf bank_mask:0xf bound_ctrl:1
	v_max_f32_e32 v6, v6, v6
	v_max_f32_e32 v3, v3, v6
	v_mov_b32_e32 v6, v3
	s_nop 1
	v_permlane16_swap_b32_e32 v3, v6
	v_max_f32 v3, v3, v6
	s_nop 1
	s_nop 0
	v_mov_b32_e32 v6, v3
	s_nop 1
	v_permlane32_swap_b32_e32 v3, v6
	v_max_f32 v3, v3, v6
	s_nop 0
	v_max_f32_e32 v3, v3, v3
	v_max_f32_e32 v3, 0xda24260, v3
	v_rcp_f32_e32 v6, v3
	s_nop 0
	v_mul_f32_e32 v6, 0x42fe0000, v6
	v_fmaak_f32 v5, v5, v6, 0x4b400000
	v_fmaak_f32 v4, v4, v6, 0x4b400000
	v_lshlrev_b32_e32 v5, 8, v5
	v_perm_b32 v4, v5, v4, s0
	s_nop 1
	v_mov_b32_dpp v5, v4 quad_perm:[1,0,3,2] row_mask:0xf bank_mask:0xf bound_ctrl:1
	s_and_saveexec_b64 s[0:1], vcc
	v_lshl_or_b32 v4, v5, 16, v4
	ds_write_b32 v1, v4 offset:3872
	s_or_b64 exec, exec, s[0:1]
	ds_read_b64 v[126:127], v1 offset:5040
	ds_read_b64 v[128:129], v1 offset:6064
	ds_read_b64 v[6:7], v1 offset:5552
	s_mov_b32 s0, 0xc0c0500
	s_waitcnt lgkmcnt(0)
; #define LAS __attribute__((address_space(3)))
; #define LDS_WAIT() asm volatile("s_waitcnt lgkmcnt(0)" ::: "memory")
;     ...
;     for (int j = 0; j < PE_NT; ++j) {
;         LAS unsigned* lt = lw + j * PE_TOK_W + 128;
;         const float a0 = __builtin_bit_cast(float, lt[2 * lane]), a1 = __builtin_bit_cast(float, lt[2 * lane + 1]);
;         const float wm = fmaxf(wave_max(fmaxf(fabsf(a0), fabsf(a1))), 1e-30f), wq = 127.0f * __builtin_amdgcn_rcpf(wm);
;         wsj[j] = wm * (1.0f / 127.0f);
;         const unsigned pr = (__builtin_bit_cast(unsigned, __builtin_fmaf(a0, wq, 12582912.0f)) & 0xffu) | ((__builtin_bit_cast(unsigned, __builtin_fmaf(a1, wq, 12582912.0f)) & 0xffu) << 8);
;         const unsigned nbp = (unsigned)__builtin_amdgcn_update_dpp(0, (int)pr, 0xB1, 0xF, 0xF, true);
;         asm volatile("" ::: "memory");
;         if ((lane & 1) == 0) lt[2 * lane] = pr | (nbp << 16);
;     }
;     LDS_WAIT(); asm volatile("" ::: "memory");
;     {
;         unsigned er[PE_RD];
; #pragma unroll
;         for (int q = 0; q < PE_RD; ++q) { const v4u rec = *(const LAS v4u*)(ents + 4 * q); er[q] = __builtin_amdgcn_readfirstlane(rec.x); PE_ISSUE4(q, rec, VB8); }
;         int curi[16];
; #pragma unroll
;         for (int i = 0; i < 16; ++i) curi[i] = 0;
;         int jcur = (int)((er[0] >> 14) & 3u);
;         v4u nrec = *(const LAS v4u*)(ents + 4 * PE_RD);
	v_cvt_f32_i32_e32 v126, v126
	v_cvt_f32_i32_e32 v127, v127
	v_mul_f32_e32 v126, v128, v126
	v_mul_f32_e32 v127, v129, v127
	v_mul_f32_e32 v94, v126, v126
	v_mul_f32_e32 v95, v127, v127
	v_fmamk_f32 v94, v94, 0xbdd2d3e8, v113
	v_fmamk_f32 v95, v95, 0xbdd2d3e8, v113
	v_mul_f32_e32 v94, v126, v94
	v_mul_f32_e32 v95, v127, v95
	v_exp_f32_e32 v94, v94
	v_exp_f32_e32 v95, v95
	s_nop 0
	v_add_f32_e32 v94, 1.0, v94
	v_add_f32_e32 v95, 1.0, v95
	v_rcp_f32_e32 v94, v94
	v_rcp_f32_e32 v95, v95
	s_nop 0
	v_mul_f32_e32 v126, v126, v94
	v_mul_f32_e32 v127, v127, v95
	v_mul_f32_e32 v6, v6, v126
	v_mul_f32_e32 v7, v7, v127
	v_max_f32_e64 v4, |v7|, |v7|
	v_max_f32_e64 v5, |v6|, |v6|
	v_max_f32_e32 v4, v5, v4
	s_nop 1
	v_mov_b32_dpp v5, v4 quad_perm:[1,0,3,2] row_mask:0xf bank_mask:0xf bound_ctrl:1
	v_max_f32_e32 v5, v5, v5
	v_max_f32_e32 v4, v4, v5
	s_nop 1
	v_mov_b32_dpp v5, v4 quad_perm:[2,3,0,1] row_mask:0xf bank_mask:0xf bound_ctrl:1
	v_max_f32_e32 v5, v5, v5
	v_max_f32_e32 v4, v4, v5
	s_nop 1
	v_mov_b32_dpp v5, v4 row_half_mirror row_mask:0xf bank_mask:0xf bound_ctrl:1
	v_max_f32_e32 v5, v5, v5
	v_max_f32_e32 v4, v4, v5
	s_nop 1
	v_mov_b32_dpp v5, v4 row_mirror row_mask:0xf bank_mask:0xf bound_ctrl:1
	v_max_f32_e32 v5, v5, v5
	v_max_f32_e32 v4, v4, v5
	v_mov_b32_e32 v5, v4
	s_nop 1
	v_permlane16_swap_b32_e32 v4, v5
	v_max_f32 v4, v4, v5
	s_nop 1
	s_nop 0
	v_mov_b32_e32 v5, v4
	s_nop 1
	v_permlane32_swap_b32_e32 v4, v5
	v_max_f32 v4, v4, v5
	s_nop 0
	v_max_f32_e32 v4, v4, v4
	v_max_f32_e32 v4, 0xda24260, v4
	v_rcp_f32_e32 v5, v4
	s_nop 0
	v_mul_f32_e32 v5, 0x42fe0000, v5
	v_fmaak_f32 v6, v6, v5, 0x4b400000
	v_fmaak_f32 v5, v7, v5, 0x4b400000
	v_lshlrev_b32_e32 v5, 8, v5
	v_perm_b32 v5, v5, v6, s0
	s_nop 1
	v_mov_b32_dpp v6, v5 quad_perm:[1,0,3,2] row_mask:0xf bank_mask:0xf bound_ctrl:1
	s_and_saveexec_b64 s[0:1], vcc
	v_lshl_or_b32 v5, v6, 16, v5
	ds_write_b32 v1, v5 offset:5552
	s_or_b64 exec, exec, s[0:1]
	s_waitcnt lgkmcnt(0)
	v_mov_b32_e32 v1, s90
	ds_read_b128 v[6:9], v1 offset:6720
	v_mul_f32_e32 v119, 0x3c010204, v3
	v_mul_f32_e32 v117, 0x3c010204, v4
	v_mul_f32_e32 v121, 0x3c010204, v0
	v_mul_f32_e32 v120, 0x3c010204, v2
	s_waitcnt lgkmcnt(0)
	v_lshlrev_b32_e32 v5, 9, v6
	v_and_b32_e32 v5, 0x7ffe00, v5
	v_add_u32_e32 v5, v5, v118
	global_load_dwordx2 v[70:71], v5, s[82:83]
	v_lshl_add_u32 v7, v7, 9, v118
	global_load_dwordx2 v[72:73], v7, s[82:83]
	v_lshl_add_u32 v8, v8, 9, v118
	global_load_dwordx2 v[74:75], v8, s[82:83]
	v_lshl_add_u32 v9, v9, 9, v118
	global_load_dwordx2 v[80:81], v9, s[82:83]
	ds_read_b128 v[8:11], v1 offset:6736
	v_readfirstlane_b32 s4, v6
	s_bfe_u32 s7, s4, 0x2000e
	s_andn2_b64 vcc, exec, s[2:3]
	s_mov_b32 s0, 0
	s_waitcnt lgkmcnt(0)
	v_lshlrev_b32_e32 v3, 9, v8
	v_and_b32_e32 v3, 0x7ffe00, v3
	v_add_u32_e32 v3, v3, v118
	global_load_dwordx2 v[76:77], v3, s[82:83]
	v_lshl_add_u32 v4, v9, 9, v118
	global_load_dwordx2 v[82:83], v4, s[82:83]
	v_lshl_add_u32 v5, v10, 9, v118
	global_load_dwordx2 v[84:85], v5, s[82:83]
	v_lshl_add_u32 v3, v11, 9, v118
	global_load_dwordx2 v[90:91], v3, s[82:83]
	ds_read_b128 v[10:13], v1 offset:6752
	v_readfirstlane_b32 s5, v8
	s_waitcnt lgkmcnt(0)
	v_lshlrev_b32_e32 v0, 9, v10
	v_and_b32_e32 v0, 0x7ffe00, v0
	v_add_u32_e32 v0, v0, v118
	global_load_dwordx2 v[78:79], v0, s[82:83]
	v_lshl_add_u32 v0, v11, 9, v118
	global_load_dwordx2 v[86:87], v0, s[82:83]
	v_lshl_add_u32 v0, v12, 9, v118
	global_load_dwordx2 v[88:89], v0, s[82:83]
	v_lshl_add_u32 v0, v13, 9, v118
	global_load_dwordx2 v[92:93], v0, s[82:83]
	v_readfirstlane_b32 s8, v10
	s_cbranch_vccnz .LBB0_2884
	v_mov_b32_e32 v48, v49
	v_mov_b32_e32 v130, 0x1010101
	v_mov_b32_e32 v131, 0
	v_mov_b32_e32 v132, 0
	v_mov_b32_e32 v133, 0
	v_mov_b32_e32 v134, 0
	v_mov_b32_e32 v94, 0
	v_mov_b32_e32 v95, 0
	v_mov_b32_e32 v96, 0
	v_mov_b32_e32 v97, 0
	v_mov_b32_e32 v98, 0
	v_mov_b32_e32 v99, 0
	v_mov_b32_e32 v100, 0
	v_mov_b32_e32 v101, 0
	v_mov_b32_e32 v102, 0
	v_mov_b32_e32 v103, 0
	v_mov_b32_e32 v104, 0
	v_mov_b32_e32 v105, 0
	v_mov_b32_e32 v106, 0
	v_mov_b32_e32 v107, 0
	v_mov_b32_e32 v108, 0
	v_mov_b32_e32 v109, 0
	v_readlane_b32 s1, v255, 2
	v_mov_b64_e32 v[12:13], v[48:49]
	v_mov_b64_e32 v[14:15], v[48:49]
	v_mov_b64_e32 v[16:17], v[48:49]
	v_mov_b64_e32 v[18:19], v[48:49]
	v_mov_b64_e32 v[34:35], v[48:49]
	v_mov_b64_e32 v[32:33], v[48:49]
	v_mov_b64_e32 v[30:31], v[48:49]
	v_mov_b64_e32 v[28:29], v[48:49]
	v_mov_b64_e32 v[26:27], v[48:49]
	v_mov_b64_e32 v[24:25], v[48:49]
	v_mov_b64_e32 v[22:23], v[48:49]
	v_mov_b64_e32 v[20:21], v[48:49]
	v_mov_b64_e32 v[52:53], v[48:49]
	v_mov_b64_e32 v[50:51], v[48:49]
	v_mov_b64_e32 v[46:47], v[48:49]
	v_mov_b64_e32 v[44:45], v[48:49]
	v_mov_b64_e32 v[42:43], v[48:49]
	v_mov_b64_e32 v[40:41], v[48:49]
	v_mov_b64_e32 v[38:39], v[48:49]
	v_mov_b64_e32 v[36:37], v[48:49]
	v_mov_b64_e32 v[68:69], v[48:49]
	v_mov_b64_e32 v[66:67], v[48:49]
	v_mov_b64_e32 v[64:65], v[48:49]
	v_mov_b64_e32 v[62:63], v[48:49]
	v_mov_b64_e32 v[60:61], v[48:49]
	v_mov_b64_e32 v[58:59], v[48:49]
	v_mov_b64_e32 v[56:57], v[48:49]
	v_mov_b64_e32 v[54:55], v[48:49]
	v_mov_b64_e32 v[10:11], v[48:49]
	v_mov_b64_e32 v[8:9], v[48:49]
	v_mov_b64_e32 v[6:7], v[48:49]
	v_mov_b64_e32 v[4:5], v[48:49]
	v_mov_b32_e32 v135, s1
	s_bfe_u32 s98, s4, 0x2000e
	s_mulk_i32 s98, 0x690
	s_lshr_b32 s99, s4, 17
	s_add_i32 s98, s90, s98
	s_and_b32 s99, s99, 0x7ffc
	s_add_i32 s98, s98, s99
	v_mov_b32_e32 v137, s98
	ds_read_b32 v137, v137 offset:512
	s_bfe_u32 s98, s5, 0x2000e
	s_mulk_i32 s98, 0x690
	s_lshr_b32 s99, s5, 17
	s_add_i32 s98, s90, s98
	s_and_b32 s99, s99, 0x7ffc
	s_add_i32 s98, s98, s99
	v_mov_b32_e32 v138, s98
	ds_read_b32 v138, v138 offset:512
	s_bfe_u32 s98, s8, 0x2000e
	s_mulk_i32 s98, 0x690
	s_lshr_b32 s99, s8, 17
	s_add_i32 s98, s90, s98
	s_and_b32 s99, s99, 0x7ffc
	s_add_i32 s98, s98, s99
	v_mov_b32_e32 v139, s98
	ds_read_b32 v139, v139 offset:512
	s_waitcnt lgkmcnt(0)
	s_branch .LBB0_2873
; #define LAS __attribute__((address_space(3)))
; #define PE_VMW "vmcnt(" PE_STR(PE_VMY) ")"
; #define PE_WAIT4U(S, cntstr) asm volatile("s_waitcnt " cntstr : "+v"(ru4[S][0]), "+v"(ru4[S][1]), "+v"(ru4[S][2]), "+v"(ru4[S][3]) :: "memory")
;     ...
;         for (int bi = 0; bi < nb; bi += PE_RD) {
; #pragma unroll
;             for (int q = 0; q < PE_RD; ++q) {
;                 PE_WAIT4U(q, PE_VMW);
;                 PE_VBATCH(q, er[q]);
;                 er[q] = __builtin_amdgcn_readfirstlane(nrec.x);
;                 PE_ISSUE4(q, nrec, VB8);
;                 nrec = *(const LAS v4u*)(ents + 4 * (bi + q + PE_RD + 1));
;             }
.LvC_t0:
	v_perm_b32 v126, v86, v78, s91
	v_perm_b32 v78, v86, v78, s92
	v_perm_b32 v86, v92, v88, s91
	v_perm_b32 v88, v92, v88, s92
	v_perm_b32 v92, v86, v126, s94
	v_perm_b32 v86, v86, v126, s68
	v_perm_b32 v126, v88, v78, s94
	v_perm_b32 v78, v88, v78, s68
	v_dot4_i32_i8 v54, v92, v139, v54
	v_dot4_i32_i8 v55, v86, v139, v55
	v_dot4_i32_i8 v56, v126, v139, v56
	v_dot4_i32_i8 v57, v78, v139, v57
	v_and_b32_e32 v86, 0xf0f0f0f0, v86
	v_and_b32_e32 v78, 0xf0f0f0f0, v78
	v_and_b32_e32 v88, 0xf0f0f0f0, v92
	v_and_b32_e32 v92, 0xf0f0f0f0, v126
	v_dot4_i32_i8 v58, v88, v139, v58
	v_dot4_i32_i8 v59, v86, v139, v59
	v_dot4_i32_i8 v60, v92, v139, v60
	v_dot4_i32_i8 v61, v78, v139, v61
	v_perm_b32 v78, v87, v79, s91
	v_perm_b32 v86, v93, v89, s91
	v_perm_b32 v79, v87, v79, s92
	v_perm_b32 v87, v93, v89, s92
	v_perm_b32 v88, v86, v78, s94
	v_perm_b32 v78, v86, v78, s68
	v_perm_b32 v86, v87, v79, s94
	v_perm_b32 v79, v87, v79, s68
	v_dot4_i32_i8 v62, v88, v139, v62
	v_dot4_i32_i8 v63, v78, v139, v63
	v_dot4_i32_i8 v64, v86, v139, v64
	v_dot4_i32_i8 v65, v79, v139, v65
	v_and_b32_e32 v87, 0xf0f0f0f0, v88
	v_and_b32_e32 v78, 0xf0f0f0f0, v78
	v_and_b32_e32 v86, 0xf0f0f0f0, v86
	v_and_b32_e32 v79, 0xf0f0f0f0, v79
	v_dot4_i32_i8 v66, v87, v139, v66
	v_dot4_i32_i8 v67, v78, v139, v67
	v_dot4_i32_i8 v68, v86, v139, v68
	v_dot4_i32_i8 v69, v79, v139, v69
	v_dot4_i32_i8 v131, v130, v139, v131
	s_branch .LBB0_2872
.LvC_t1:
	v_perm_b32 v126, v86, v78, s91
	v_perm_b32 v78, v86, v78, s92
	v_perm_b32 v86, v92, v88, s91
	v_perm_b32 v88, v92, v88, s92
	v_perm_b32 v92, v86, v126, s94
	v_perm_b32 v86, v86, v126, s68
	v_perm_b32 v126, v88, v78, s94
	v_perm_b32 v78, v88, v78, s68
	v_dot4_i32_i8 v36, v92, v139, v36
	v_dot4_i32_i8 v37, v86, v139, v37
	v_dot4_i32_i8 v38, v126, v139, v38
	v_dot4_i32_i8 v39, v78, v139, v39
	v_and_b32_e32 v86, 0xf0f0f0f0, v86
	v_and_b32_e32 v78, 0xf0f0f0f0, v78
	v_and_b32_e32 v88, 0xf0f0f0f0, v92
	v_and_b32_e32 v92, 0xf0f0f0f0, v126
	v_dot4_i32_i8 v40, v88, v139, v40
	v_dot4_i32_i8 v41, v86, v139, v41
	v_dot4_i32_i8 v42, v92, v139, v42
	v_dot4_i32_i8 v43, v78, v139, v43
	v_perm_b32 v78, v87, v79, s91
	v_perm_b32 v86, v93, v89, s91
	v_perm_b32 v79, v87, v79, s92
	v_perm_b32 v87, v93, v89, s92
	v_perm_b32 v88, v86, v78, s94
	v_perm_b32 v78, v86, v78, s68
	v_perm_b32 v86, v87, v79, s94
	v_perm_b32 v79, v87, v79, s68
	v_dot4_i32_i8 v44, v88, v139, v44
	v_dot4_i32_i8 v45, v78, v139, v45
	v_dot4_i32_i8 v46, v86, v139, v46
	v_dot4_i32_i8 v47, v79, v139, v47
	v_and_b32_e32 v87, 0xf0f0f0f0, v88
	v_and_b32_e32 v78, 0xf0f0f0f0, v78
	v_and_b32_e32 v86, 0xf0f0f0f0, v86
	v_and_b32_e32 v79, 0xf0f0f0f0, v79
	v_dot4_i32_i8 v50, v87, v139, v50
	v_dot4_i32_i8 v51, v78, v139, v51
	v_dot4_i32_i8 v52, v86, v139, v52
	v_dot4_i32_i8 v53, v79, v139, v53
	v_dot4_i32_i8 v132, v130, v139, v132
	s_branch .LBB0_2872
.LvC_t2:
	v_perm_b32 v126, v86, v78, s91
	v_perm_b32 v78, v86, v78, s92
	v_perm_b32 v86, v92, v88, s91
	v_perm_b32 v88, v92, v88, s92
	v_perm_b32 v92, v86, v126, s94
	v_perm_b32 v86, v86, v126, s68
	v_perm_b32 v126, v88, v78, s94
	v_perm_b32 v78, v88, v78, s68
	v_dot4_i32_i8 v20, v92, v139, v20
	v_dot4_i32_i8 v21, v86, v139, v21
	v_dot4_i32_i8 v22, v126, v139, v22
	v_dot4_i32_i8 v23, v78, v139, v23
	v_and_b32_e32 v86, 0xf0f0f0f0, v86
	v_and_b32_e32 v78, 0xf0f0f0f0, v78
	v_and_b32_e32 v88, 0xf0f0f0f0, v92
	v_and_b32_e32 v92, 0xf0f0f0f0, v126
	v_dot4_i32_i8 v24, v88, v139, v24
	v_dot4_i32_i8 v25, v86, v139, v25
	v_dot4_i32_i8 v26, v92, v139, v26
	v_dot4_i32_i8 v27, v78, v139, v27
	v_perm_b32 v78, v87, v79, s91
	v_perm_b32 v86, v93, v89, s91
	v_perm_b32 v79, v87, v79, s92
	v_perm_b32 v87, v93, v89, s92
	v_perm_b32 v88, v86, v78, s94
	v_perm_b32 v78, v86, v78, s68
	v_perm_b32 v86, v87, v79, s94
	v_perm_b32 v79, v87, v79, s68
	v_dot4_i32_i8 v28, v88, v139, v28
	v_dot4_i32_i8 v29, v78, v139, v29
	v_dot4_i32_i8 v30, v86, v139, v30
	v_dot4_i32_i8 v31, v79, v139, v31
	v_and_b32_e32 v87, 0xf0f0f0f0, v88
	v_and_b32_e32 v78, 0xf0f0f0f0, v78
	v_and_b32_e32 v86, 0xf0f0f0f0, v86
	v_and_b32_e32 v79, 0xf0f0f0f0, v79
	v_dot4_i32_i8 v32, v87, v139, v32
	v_dot4_i32_i8 v33, v78, v139, v33
	v_dot4_i32_i8 v34, v86, v139, v34
	v_dot4_i32_i8 v35, v79, v139, v35
	v_dot4_i32_i8 v133, v130, v139, v133
	s_branch .LBB0_2872
.LvC_t3:
	v_perm_b32 v126, v86, v78, s91
	v_perm_b32 v78, v86, v78, s92
	v_perm_b32 v86, v92, v88, s91
	v_perm_b32 v88, v92, v88, s92
	v_perm_b32 v92, v86, v126, s94
	v_perm_b32 v86, v86, v126, s68
	v_perm_b32 v126, v88, v78, s94
	v_perm_b32 v78, v88, v78, s68
	v_dot4_i32_i8 v18, v92, v139, v18
	v_dot4_i32_i8 v19, v86, v139, v19
	v_dot4_i32_i8 v16, v126, v139, v16
	v_dot4_i32_i8 v17, v78, v139, v17
	v_and_b32_e32 v86, 0xf0f0f0f0, v86
	v_and_b32_e32 v78, 0xf0f0f0f0, v78
	v_and_b32_e32 v88, 0xf0f0f0f0, v92
	v_and_b32_e32 v92, 0xf0f0f0f0, v126
	v_dot4_i32_i8 v14, v88, v139, v14
	v_dot4_i32_i8 v15, v86, v139, v15
	v_dot4_i32_i8 v12, v92, v139, v12
	v_dot4_i32_i8 v13, v78, v139, v13
	v_perm_b32 v78, v87, v79, s91
	v_perm_b32 v86, v93, v89, s91
	v_perm_b32 v79, v87, v79, s92
	v_perm_b32 v87, v93, v89, s92
	v_perm_b32 v88, v86, v78, s94
	v_perm_b32 v78, v86, v78, s68
	v_perm_b32 v86, v87, v79, s94
	v_perm_b32 v79, v87, v79, s68
	v_dot4_i32_i8 v10, v88, v139, v10
	v_dot4_i32_i8 v11, v78, v139, v11
	v_dot4_i32_i8 v8, v86, v139, v8
	v_dot4_i32_i8 v9, v79, v139, v9
	v_and_b32_e32 v87, 0xf0f0f0f0, v88
	v_and_b32_e32 v78, 0xf0f0f0f0, v78
	v_and_b32_e32 v86, 0xf0f0f0f0, v86
	v_and_b32_e32 v79, 0xf0f0f0f0, v79
	v_dot4_i32_i8 v6, v87, v139, v6
	v_dot4_i32_i8 v7, v78, v139, v7
	v_dot4_i32_i8 v4, v86, v139, v4
	v_dot4_i32_i8 v5, v79, v139, v5
	v_dot4_i32_i8 v134, v130, v139, v134
.LBB0_2872:
	s_waitcnt lgkmcnt(0)
	v_readfirstlane_b32 s8, v0
	s_bfe_u32 s98, s8, 0x2000e
	s_mulk_i32 s98, 0x690
	s_lshr_b32 s99, s8, 17
	s_add_i32 s98, s90, s98
	s_and_b32 s99, s99, 0x7ffc
	s_add_i32 s98, s98, s99
	v_mov_b32_e32 v139, s98
	ds_read_b32 v139, v139 offset:512
	v_and_b32_e32 v0, 0x3fff, v0
	v_lshl_add_u32 v0, v0, 9, v118
	global_load_dwordx2 v[78:79], v0, s[82:83]
	v_lshl_add_u32 v0, v1, 9, v118
	global_load_dwordx2 v[86:87], v0, s[82:83]
	v_lshl_add_u32 v0, v2, 9, v118
	global_load_dwordx2 v[88:89], v0, s[82:83]
	v_lshl_add_u32 v0, v3, 9, v118
	global_load_dwordx2 v[92:93], v0, s[82:83]
	s_add_i32 s0, s0, 3
	s_add_i32 s1, s1, 48
	v_add_u32_e32 v135, 48, v135
	s_cmp_ge_i32 s0, s6
	s_cbranch_scc1 .LBB0_2677

.LvA_t0:
	v_perm_b32 v126, v72, v70, s91
	v_perm_b32 v70, v72, v70, s92
	v_perm_b32 v72, v80, v74, s91
	v_perm_b32 v74, v80, v74, s92
	v_perm_b32 v80, v72, v126, s94
	v_perm_b32 v72, v72, v126, s68
	v_perm_b32 v126, v74, v70, s94
	v_perm_b32 v70, v74, v70, s68
	v_dot4_i32_i8 v54, v80, v137, v54
	v_dot4_i32_i8 v55, v72, v137, v55
	v_dot4_i32_i8 v56, v126, v137, v56
	v_dot4_i32_i8 v57, v70, v137, v57
	v_and_b32_e32 v72, 0xf0f0f0f0, v72
	v_and_b32_e32 v70, 0xf0f0f0f0, v70
	v_and_b32_e32 v74, 0xf0f0f0f0, v80
	v_and_b32_e32 v80, 0xf0f0f0f0, v126
	v_dot4_i32_i8 v58, v74, v137, v58
	v_dot4_i32_i8 v59, v72, v137, v59
	v_dot4_i32_i8 v60, v80, v137, v60
	v_dot4_i32_i8 v61, v70, v137, v61
	v_perm_b32 v70, v73, v71, s91
	v_perm_b32 v72, v81, v75, s91
	v_perm_b32 v71, v73, v71, s92
	v_perm_b32 v73, v81, v75, s92
	v_perm_b32 v74, v72, v70, s94
	v_perm_b32 v70, v72, v70, s68
	v_perm_b32 v72, v73, v71, s94
	v_perm_b32 v71, v73, v71, s68
	v_dot4_i32_i8 v62, v74, v137, v62
	v_dot4_i32_i8 v63, v70, v137, v63
	v_dot4_i32_i8 v64, v72, v137, v64
	v_dot4_i32_i8 v65, v71, v137, v65
	v_and_b32_e32 v73, 0xf0f0f0f0, v74
	v_and_b32_e32 v70, 0xf0f0f0f0, v70
	v_and_b32_e32 v72, 0xf0f0f0f0, v72
	v_and_b32_e32 v71, 0xf0f0f0f0, v71
	v_dot4_i32_i8 v66, v73, v137, v66
	v_dot4_i32_i8 v67, v70, v137, v67
	v_dot4_i32_i8 v68, v72, v137, v68
	v_dot4_i32_i8 v69, v71, v137, v69
	v_dot4_i32_i8 v131, v130, v137, v131
	s_branch .LBB0_2877
.LvA_t1:
	v_perm_b32 v126, v72, v70, s91
	v_perm_b32 v70, v72, v70, s92
	v_perm_b32 v72, v80, v74, s91
	v_perm_b32 v74, v80, v74, s92
	v_perm_b32 v80, v72, v126, s94
	v_perm_b32 v72, v72, v126, s68
	v_perm_b32 v126, v74, v70, s94
	v_perm_b32 v70, v74, v70, s68
	v_dot4_i32_i8 v36, v80, v137, v36
	v_dot4_i32_i8 v37, v72, v137, v37
	v_dot4_i32_i8 v38, v126, v137, v38
	v_dot4_i32_i8 v39, v70, v137, v39
	v_and_b32_e32 v72, 0xf0f0f0f0, v72
	v_and_b32_e32 v70, 0xf0f0f0f0, v70
	v_and_b32_e32 v74, 0xf0f0f0f0, v80
	v_and_b32_e32 v80, 0xf0f0f0f0, v126
	v_dot4_i32_i8 v40, v74, v137, v40
	v_dot4_i32_i8 v41, v72, v137, v41
	v_dot4_i32_i8 v42, v80, v137, v42
	v_dot4_i32_i8 v43, v70, v137, v43
	v_perm_b32 v70, v73, v71, s91
	v_perm_b32 v72, v81, v75, s91
	v_perm_b32 v71, v73, v71, s92
	v_perm_b32 v73, v81, v75, s92
	v_perm_b32 v74, v72, v70, s94
	v_perm_b32 v70, v72, v70, s68
	v_perm_b32 v72, v73, v71, s94
	v_perm_b32 v71, v73, v71, s68
	v_dot4_i32_i8 v44, v74, v137, v44
	v_dot4_i32_i8 v45, v70, v137, v45
	v_dot4_i32_i8 v46, v72, v137, v46
	v_dot4_i32_i8 v47, v71, v137, v47
	v_and_b32_e32 v73, 0xf0f0f0f0, v74
	v_and_b32_e32 v70, 0xf0f0f0f0, v70
	v_and_b32_e32 v72, 0xf0f0f0f0, v72
	v_and_b32_e32 v71, 0xf0f0f0f0, v71
	v_dot4_i32_i8 v50, v73, v137, v50
	v_dot4_i32_i8 v51, v70, v137, v51
	v_dot4_i32_i8 v52, v72, v137, v52
	v_dot4_i32_i8 v53, v71, v137, v53
	v_dot4_i32_i8 v132, v130, v137, v132
	s_branch .LBB0_2877
.LvA_t2:
	v_perm_b32 v126, v72, v70, s91
	v_perm_b32 v70, v72, v70, s92
	v_perm_b32 v72, v80, v74, s91
	v_perm_b32 v74, v80, v74, s92
	v_perm_b32 v80, v72, v126, s94
	v_perm_b32 v72, v72, v126, s68
	v_perm_b32 v126, v74, v70, s94
	v_perm_b32 v70, v74, v70, s68
	v_dot4_i32_i8 v20, v80, v137, v20
	v_dot4_i32_i8 v21, v72, v137, v21
	v_dot4_i32_i8 v22, v126, v137, v22
	v_dot4_i32_i8 v23, v70, v137, v23
	v_and_b32_e32 v72, 0xf0f0f0f0, v72
	v_and_b32_e32 v70, 0xf0f0f0f0, v70
	v_and_b32_e32 v74, 0xf0f0f0f0, v80
	v_and_b32_e32 v80, 0xf0f0f0f0, v126
	v_dot4_i32_i8 v24, v74, v137, v24
	v_dot4_i32_i8 v25, v72, v137, v25
	v_dot4_i32_i8 v26, v80, v137, v26
	v_dot4_i32_i8 v27, v70, v137, v27
	v_perm_b32 v70, v73, v71, s91
	v_perm_b32 v72, v81, v75, s91
	v_perm_b32 v71, v73, v71, s92
	v_perm_b32 v73, v81, v75, s92
	v_perm_b32 v74, v72, v70, s94
	v_perm_b32 v70, v72, v70, s68
	v_perm_b32 v72, v73, v71, s94
	v_perm_b32 v71, v73, v71, s68
	v_dot4_i32_i8 v28, v74, v137, v28
	v_dot4_i32_i8 v29, v70, v137, v29
	v_dot4_i32_i8 v30, v72, v137, v30
	v_dot4_i32_i8 v31, v71, v137, v31
	v_and_b32_e32 v73, 0xf0f0f0f0, v74
	v_and_b32_e32 v70, 0xf0f0f0f0, v70
	v_and_b32_e32 v72, 0xf0f0f0f0, v72
	v_and_b32_e32 v71, 0xf0f0f0f0, v71
	v_dot4_i32_i8 v32, v73, v137, v32
	v_dot4_i32_i8 v33, v70, v137, v33
	v_dot4_i32_i8 v34, v72, v137, v34
	v_dot4_i32_i8 v35, v71, v137, v35
	v_dot4_i32_i8 v133, v130, v137, v133
	s_branch .LBB0_2877
.LvA_t3:
	v_perm_b32 v126, v72, v70, s91
	v_perm_b32 v70, v72, v70, s92
	v_perm_b32 v72, v80, v74, s91
	v_perm_b32 v74, v80, v74, s92
	v_perm_b32 v80, v72, v126, s94
	v_perm_b32 v72, v72, v126, s68
	v_perm_b32 v126, v74, v70, s94
	v_perm_b32 v70, v74, v70, s68
	v_dot4_i32_i8 v18, v80, v137, v18
	v_dot4_i32_i8 v19, v72, v137, v19
	v_dot4_i32_i8 v16, v126, v137, v16
	v_dot4_i32_i8 v17, v70, v137, v17
	v_and_b32_e32 v72, 0xf0f0f0f0, v72
	v_and_b32_e32 v70, 0xf0f0f0f0, v70
	v_and_b32_e32 v74, 0xf0f0f0f0, v80
	v_and_b32_e32 v80, 0xf0f0f0f0, v126
	v_dot4_i32_i8 v14, v74, v137, v14
	v_dot4_i32_i8 v15, v72, v137, v15
	v_dot4_i32_i8 v12, v80, v137, v12
	v_dot4_i32_i8 v13, v70, v137, v13
	v_perm_b32 v70, v73, v71, s91
	v_perm_b32 v72, v81, v75, s91
	v_perm_b32 v71, v73, v71, s92
	v_perm_b32 v73, v81, v75, s92
	v_perm_b32 v74, v72, v70, s94
	v_perm_b32 v70, v72, v70, s68
	v_perm_b32 v72, v73, v71, s94
	v_perm_b32 v71, v73, v71, s68
	v_dot4_i32_i8 v10, v74, v137, v10
	v_dot4_i32_i8 v11, v70, v137, v11
	v_dot4_i32_i8 v8, v72, v137, v8
	v_dot4_i32_i8 v9, v71, v137, v9
	v_and_b32_e32 v73, 0xf0f0f0f0, v74
	v_and_b32_e32 v70, 0xf0f0f0f0, v70
	v_and_b32_e32 v72, 0xf0f0f0f0, v72
	v_and_b32_e32 v71, 0xf0f0f0f0, v71
	v_dot4_i32_i8 v6, v73, v137, v6
	v_dot4_i32_i8 v7, v70, v137, v7
	v_dot4_i32_i8 v4, v72, v137, v4
	v_dot4_i32_i8 v5, v71, v137, v5
	v_dot4_i32_i8 v134, v130, v137, v134
; #define LAS __attribute__((address_space(3)))
; #define PE_VMW "vmcnt(" PE_STR(PE_VMY) ")"
; #define PE_WAIT4U(S, cntstr) asm volatile("s_waitcnt " cntstr : "+v"(ru4[S][0]), "+v"(ru4[S][1]), "+v"(ru4[S][2]), "+v"(ru4[S][3]) :: "memory")
;     ...
;         for (int bi = 0; bi < nb; bi += PE_RD) {
; #pragma unroll
;             for (int q = 0; q < PE_RD; ++q) {
;                 PE_WAIT4U(q, PE_VMW);
;                 PE_VBATCH(q, er[q]);
;                 er[q] = __builtin_amdgcn_readfirstlane(nrec.x);
;                 PE_ISSUE4(q, nrec, VB8);
;                 nrec = *(const LAS v4u*)(ents + 4 * (bi + q + PE_RD + 1));
.LBB0_2877:
	s_waitcnt lgkmcnt(0)
	v_readfirstlane_b32 s4, v0
	s_bfe_u32 s98, s4, 0x2000e
	s_mulk_i32 s98, 0x690
	s_lshr_b32 s99, s4, 17
	s_add_i32 s98, s90, s98
	s_and_b32 s99, s99, 0x7ffc
	s_add_i32 s98, s98, s99
	v_mov_b32_e32 v137, s98
	ds_read_b32 v137, v137 offset:512
	v_and_b32_e32 v0, 0x3fff, v0
	v_lshl_add_u32 v0, v0, 9, v118
	global_load_dwordx2 v[70:71], v0, s[82:83]
	v_lshl_add_u32 v0, v1, 9, v118
	global_load_dwordx2 v[72:73], v0, s[82:83]
	v_lshl_add_u32 v0, v2, 9, v118
	global_load_dwordx2 v[74:75], v0, s[82:83]
	v_lshl_add_u32 v0, v3, 9, v118
	global_load_dwordx2 v[80:81], v0, s[82:83]
	ds_read_b128 v[0:3], v135 offset:16
	s_waitcnt vmcnt(8)
	s_and_b32 s2, s5, 0x70000
	s_cmp_eq_u32 s2, 0
	s_cbranch_scc1 .LBB0_2881
	s_bfe_u32 s2, s5, 0x2000e
	s_cmp_eq_u32 s2, 0
	s_cbranch_scc1 .LvB_t0
	s_cmp_eq_u32 s2, 1
	s_cbranch_scc1 .LvB_t1
	s_cmp_eq_u32 s2, 2
	s_cbranch_scc1 .LvB_t2
	s_branch .LvB_t3
.LvB_t0:
	v_perm_b32 v126, v82, v76, s91
	v_perm_b32 v76, v82, v76, s92
	v_perm_b32 v82, v90, v84, s91
	v_perm_b32 v84, v90, v84, s92
	v_perm_b32 v90, v82, v126, s94
	v_perm_b32 v82, v82, v126, s68
	v_perm_b32 v126, v84, v76, s94
	v_perm_b32 v76, v84, v76, s68
	v_dot4_i32_i8 v54, v90, v138, v54
	v_dot4_i32_i8 v55, v82, v138, v55
	v_dot4_i32_i8 v56, v126, v138, v56
	v_dot4_i32_i8 v57, v76, v138, v57
	v_and_b32_e32 v82, 0xf0f0f0f0, v82
	v_and_b32_e32 v76, 0xf0f0f0f0, v76
	v_and_b32_e32 v84, 0xf0f0f0f0, v90
	v_and_b32_e32 v90, 0xf0f0f0f0, v126
	v_dot4_i32_i8 v58, v84, v138, v58
	v_dot4_i32_i8 v59, v82, v138, v59
	v_dot4_i32_i8 v60, v90, v138, v60
	v_dot4_i32_i8 v61, v76, v138, v61
	v_perm_b32 v76, v83, v77, s91
	v_perm_b32 v82, v91, v85, s91
	v_perm_b32 v77, v83, v77, s92
	v_perm_b32 v83, v91, v85, s92
	v_perm_b32 v84, v82, v76, s94
	v_perm_b32 v76, v82, v76, s68
	v_perm_b32 v82, v83, v77, s94
	v_perm_b32 v77, v83, v77, s68
	v_dot4_i32_i8 v62, v84, v138, v62
	v_dot4_i32_i8 v63, v76, v138, v63
	v_dot4_i32_i8 v64, v82, v138, v64
	v_dot4_i32_i8 v65, v77, v138, v65
	v_and_b32_e32 v83, 0xf0f0f0f0, v84
	v_and_b32_e32 v76, 0xf0f0f0f0, v76
	v_and_b32_e32 v82, 0xf0f0f0f0, v82
	v_and_b32_e32 v77, 0xf0f0f0f0, v77
	v_dot4_i32_i8 v66, v83, v138, v66
	v_dot4_i32_i8 v67, v76, v138, v67
	v_dot4_i32_i8 v68, v82, v138, v68
	v_dot4_i32_i8 v69, v77, v138, v69
	v_dot4_i32_i8 v131, v130, v138, v131
	s_branch .LBB0_2881
.LvB_t1:
	v_perm_b32 v126, v82, v76, s91
	v_perm_b32 v76, v82, v76, s92
	v_perm_b32 v82, v90, v84, s91
	v_perm_b32 v84, v90, v84, s92
	v_perm_b32 v90, v82, v126, s94
	v_perm_b32 v82, v82, v126, s68
	v_perm_b32 v126, v84, v76, s94
	v_perm_b32 v76, v84, v76, s68
	v_dot4_i32_i8 v36, v90, v138, v36
	v_dot4_i32_i8 v37, v82, v138, v37
	v_dot4_i32_i8 v38, v126, v138, v38
	v_dot4_i32_i8 v39, v76, v138, v39
	v_and_b32_e32 v82, 0xf0f0f0f0, v82
	v_and_b32_e32 v76, 0xf0f0f0f0, v76
	v_and_b32_e32 v84, 0xf0f0f0f0, v90
	v_and_b32_e32 v90, 0xf0f0f0f0, v126
	v_dot4_i32_i8 v40, v84, v138, v40
	v_dot4_i32_i8 v41, v82, v138, v41
	v_dot4_i32_i8 v42, v90, v138, v42
	v_dot4_i32_i8 v43, v76, v138, v43
	v_perm_b32 v76, v83, v77, s91
	v_perm_b32 v82, v91, v85, s91
	v_perm_b32 v77, v83, v77, s92
	v_perm_b32 v83, v91, v85, s92
	v_perm_b32 v84, v82, v76, s94
	v_perm_b32 v76, v82, v76, s68
	v_perm_b32 v82, v83, v77, s94
	v_perm_b32 v77, v83, v77, s68
	v_dot4_i32_i8 v44, v84, v138, v44
	v_dot4_i32_i8 v45, v76, v138, v45
	v_dot4_i32_i8 v46, v82, v138, v46
	v_dot4_i32_i8 v47, v77, v138, v47
	v_and_b32_e32 v83, 0xf0f0f0f0, v84
	v_and_b32_e32 v76, 0xf0f0f0f0, v76
	v_and_b32_e32 v82, 0xf0f0f0f0, v82
	v_and_b32_e32 v77, 0xf0f0f0f0, v77
	v_dot4_i32_i8 v50, v83, v138, v50
	v_dot4_i32_i8 v51, v76, v138, v51
	v_dot4_i32_i8 v52, v82, v138, v52
	v_dot4_i32_i8 v53, v77, v138, v53
	v_dot4_i32_i8 v132, v130, v138, v132
	s_branch .LBB0_2881
; #define LAS __attribute__((address_space(3)))
; #define PE_VMW "vmcnt(" PE_STR(PE_VMY) ")"
; #define PE_WAIT4U(S, cntstr) asm volatile("s_waitcnt " cntstr : "+v"(ru4[S][0]), "+v"(ru4[S][1]), "+v"(ru4[S][2]), "+v"(ru4[S][3]) :: "memory")
;     ...
;         for (int bi = 0; bi < nb; bi += PE_RD) {
; #pragma unroll
;             for (int q = 0; q < PE_RD; ++q) {
;                 PE_WAIT4U(q, PE_VMW);
;                 PE_VBATCH(q, er[q]);
;                 er[q] = __builtin_amdgcn_readfirstlane(nrec.x);
;                 PE_ISSUE4(q, nrec, VB8);
;                 nrec = *(const LAS v4u*)(ents + 4 * (bi + q + PE_RD + 1));
.LvB_t2:
	v_perm_b32 v126, v82, v76, s91
	v_perm_b32 v76, v82, v76, s92
	v_perm_b32 v82, v90, v84, s91
	v_perm_b32 v84, v90, v84, s92
	v_perm_b32 v90, v82, v126, s94
	v_perm_b32 v82, v82, v126, s68
	v_perm_b32 v126, v84, v76, s94
	v_perm_b32 v76, v84, v76, s68
	v_dot4_i32_i8 v20, v90, v138, v20
	v_dot4_i32_i8 v21, v82, v138, v21
	v_dot4_i32_i8 v22, v126, v138, v22
	v_dot4_i32_i8 v23, v76, v138, v23
	v_and_b32_e32 v82, 0xf0f0f0f0, v82
	v_and_b32_e32 v76, 0xf0f0f0f0, v76
	v_and_b32_e32 v84, 0xf0f0f0f0, v90
	v_and_b32_e32 v90, 0xf0f0f0f0, v126
	v_dot4_i32_i8 v24, v84, v138, v24
	v_dot4_i32_i8 v25, v82, v138, v25
	v_dot4_i32_i8 v26, v90, v138, v26
	v_dot4_i32_i8 v27, v76, v138, v27
	v_perm_b32 v76, v83, v77, s91
	v_perm_b32 v82, v91, v85, s91
	v_perm_b32 v77, v83, v77, s92
	v_perm_b32 v83, v91, v85, s92
	v_perm_b32 v84, v82, v76, s94
	v_perm_b32 v76, v82, v76, s68
	v_perm_b32 v82, v83, v77, s94
	v_perm_b32 v77, v83, v77, s68
	v_dot4_i32_i8 v28, v84, v138, v28
	v_dot4_i32_i8 v29, v76, v138, v29
	v_dot4_i32_i8 v30, v82, v138, v30
	v_dot4_i32_i8 v31, v77, v138, v31
	v_and_b32_e32 v83, 0xf0f0f0f0, v84
	v_and_b32_e32 v76, 0xf0f0f0f0, v76
	v_and_b32_e32 v82, 0xf0f0f0f0, v82
	v_and_b32_e32 v77, 0xf0f0f0f0, v77
	v_dot4_i32_i8 v32, v83, v138, v32
	v_dot4_i32_i8 v33, v76, v138, v33
	v_dot4_i32_i8 v34, v82, v138, v34
	v_dot4_i32_i8 v35, v77, v138, v35
	v_dot4_i32_i8 v133, v130, v138, v133
	s_branch .LBB0_2881
.LvB_t3:
	v_perm_b32 v126, v82, v76, s91
	v_perm_b32 v76, v82, v76, s92
	v_perm_b32 v82, v90, v84, s91
	v_perm_b32 v84, v90, v84, s92
	v_perm_b32 v90, v82, v126, s94
	v_perm_b32 v82, v82, v126, s68
	v_perm_b32 v126, v84, v76, s94
	v_perm_b32 v76, v84, v76, s68
	v_dot4_i32_i8 v18, v90, v138, v18
	v_dot4_i32_i8 v19, v82, v138, v19
	v_dot4_i32_i8 v16, v126, v138, v16
	v_dot4_i32_i8 v17, v76, v138, v17
	v_and_b32_e32 v82, 0xf0f0f0f0, v82
	v_and_b32_e32 v76, 0xf0f0f0f0, v76
	v_and_b32_e32 v84, 0xf0f0f0f0, v90
	v_and_b32_e32 v90, 0xf0f0f0f0, v126
	v_dot4_i32_i8 v14, v84, v138, v14
	v_dot4_i32_i8 v15, v82, v138, v15
	v_dot4_i32_i8 v12, v90, v138, v12
	v_dot4_i32_i8 v13, v76, v138, v13
	v_perm_b32 v76, v83, v77, s91
	v_perm_b32 v82, v91, v85, s91
	v_perm_b32 v77, v83, v77, s92
	v_perm_b32 v83, v91, v85, s92
	v_perm_b32 v84, v82, v76, s94
	v_perm_b32 v76, v82, v76, s68
	v_perm_b32 v82, v83, v77, s94
	v_perm_b32 v77, v83, v77, s68
	v_dot4_i32_i8 v10, v84, v138, v10
	v_dot4_i32_i8 v11, v76, v138, v11
	v_dot4_i32_i8 v8, v82, v138, v8
	v_dot4_i32_i8 v9, v77, v138, v9
	v_and_b32_e32 v83, 0xf0f0f0f0, v84
	v_and_b32_e32 v76, 0xf0f0f0f0, v76
	v_and_b32_e32 v82, 0xf0f0f0f0, v82
	v_and_b32_e32 v77, 0xf0f0f0f0, v77
	v_dot4_i32_i8 v6, v83, v138, v6
	v_dot4_i32_i8 v7, v76, v138, v7
	v_dot4_i32_i8 v4, v82, v138, v4
	v_dot4_i32_i8 v5, v77, v138, v5
	v_dot4_i32_i8 v134, v130, v138, v134
.LBB0_2881:
	s_waitcnt lgkmcnt(0)
	v_readfirstlane_b32 s5, v0
	s_bfe_u32 s98, s5, 0x2000e
	s_mulk_i32 s98, 0x690
	s_lshr_b32 s99, s5, 17
	s_add_i32 s98, s90, s98
	s_and_b32 s99, s99, 0x7ffc
	s_add_i32 s98, s98, s99
	v_mov_b32_e32 v138, s98
	ds_read_b32 v138, v138 offset:512
	v_and_b32_e32 v0, 0x3fff, v0
	v_lshl_add_u32 v0, v0, 9, v118
	global_load_dwordx2 v[76:77], v0, s[82:83]
	v_lshl_add_u32 v0, v1, 9, v118
	global_load_dwordx2 v[82:83], v0, s[82:83]
	v_lshl_add_u32 v0, v2, 9, v118
	global_load_dwordx2 v[84:85], v0, s[82:83]
	v_lshl_add_u32 v0, v3, 9, v118
	global_load_dwordx2 v[90:91], v0, s[82:83]
	ds_read_b128 v[0:3], v135 offset:32
	s_waitcnt vmcnt(8)
	s_and_b32 s2, s8, 0x70000
	s_cmp_eq_u32 s2, 0
	s_cbranch_scc1 .LBB0_2872
	s_bfe_u32 s2, s8, 0x2000e
	s_cmp_eq_u32 s2, 0
	s_cbranch_scc1 .LvC_t0
	s_cmp_eq_u32 s2, 1
	s_cbranch_scc1 .LvC_t1
	s_cmp_eq_u32 s2, 2
	s_cbranch_scc1 .LvC_t2
	s_branch .LvC_t3
